# pf1: dpp6 + second attention pass's Q rows and first K/V tile requested during the first pass's tail (scalar-base loads into the idle staging registers)
# baseline (speedup 1.0000x reference)
; __device__ __forceinline__ int v_st(int k, int c) { const int kk = (k & ~0xC) | ((k & 4) << 1) | ((k & 8) >> 1); return ((kk >> 3) * 4 + (c >> 5)) * 512 + ((kk & 7) * 32 + (c & 31)) * 2; }
; __device__ __forceinline__ int v_rd_base(int lane) { return ((lane & 3) << 3) | (((lane >> 2) & 3) << 6) | (((lane >> 4) & 1) << 5) | (((lane >> 5) & 1) << 8); }
; __device__ __forceinline__ void diff_pass(const bf16_t* __restrict__ Qb, const bf16_t* __restrict__ Kh, const bf16_t* __restrict__ Vh, int seq, char* lds, f32x16 (&o)[4], const int wave_) {
;     ...
;     const bf16_t* Qw = Qb + (size_t)(wid * 32 + r32) * DM + hi * 8;
; #pragma unroll
;     for (int d0 = 0; d0 < 4; ++d0) qr[d0] = *reinterpret_cast<const bf16x8*>(Qw + d0 * 16);
;     const int sr = tid >> 4, sc = (tid & 15) * 8, vst0 = v_st(sr, sc), vst1 = v_st(32 + sr, sc);
;     const int kr = tid >> 3, kc = (tid & 7) * 8, kst = kswz<64>(kr, kc * 2);
;     const int vb0 = (int)(uintptr_t)V_lds + v_rd_base(lane);
;     bf16x8 vs0, vs1, ks;
.LBB0_838:
	v_lshrrev_b32_e32 v194, 4, v207
	v_and_b32_e32 v195, 15, v207
	v_lshlrev_b32_e32 v194, 11, v194
	v_lshl_or_b32 v194, v195, 4, v194
	global_load_dwordx4 v[178:181], v194, s[30:31]
	v_add_u32_e32 v195, 0x10000, v194
	global_load_dwordx4 v[182:185], v195, s[30:31]
	v_lshrrev_b32_e32 v194, 3, v207
	v_and_b32_e32 v195, 7, v207
	v_lshlrev_b32_e32 v194, 11, v194
	v_lshl_or_b32 v194, v195, 4, v194
	global_load_dwordx4 v[186:189], v194, s[28:29] offset:128
	v_mov_b64_e32 v[64:65], v[80:81]
	v_mov_b64_e32 v[66:67], v[82:83]
	v_mov_b64_e32 v[68:69], v[84:85]
	v_mov_b64_e32 v[70:71], v[86:87]
	v_mov_b64_e32 v[72:73], v[88:89]
	v_mov_b64_e32 v[74:75], v[90:91]
	v_mov_b64_e32 v[76:77], v[92:93]
	v_mov_b64_e32 v[78:79], v[94:95]
	ds_read_b128 v[128:131], v222 offset:61440
	ds_read_b128 v[132:135], v222 offset:57344
	v_exp_f32_e32 v124, v124
	v_exp_f32_e32 v125, v125
	v_exp_f32_e32 v126, v126
	v_exp_f32_e32 v127, v127
	s_waitcnt lgkmcnt(0)
	v_mfma_f32_32x32x16_bf16 v[80:95], v[132:135], v[162:165], v[64:79]
	ds_read_b128 v[132:135], v224 offset:61440
	ds_read_b128 v[136:139], v224 offset:57344
	s_waitcnt lgkmcnt(0)
	v_mfma_f32_32x32x16_bf16 v[80:95], v[136:139], v[166:169], v[80:95]
	ds_read_b128 v[136:139], v225 offset:61440
	ds_read_b128 v[140:143], v225 offset:57344
	v_mfma_f32_32x32x16_bf16 v[64:79], v[128:131], v[162:165], v[64:79]
	v_add_f32_e32 v128, v110, v111
	v_add_f32_e32 v129, v114, v115
	s_waitcnt lgkmcnt(0)
	v_mfma_f32_32x32x16_bf16 v[80:95], v[140:143], v[170:173], v[80:95]
	ds_read_b128 v[140:143], v227 offset:61440
	ds_read_b128 v[144:147], v227 offset:57344
	v_mfma_f32_32x32x16_bf16 v[64:79], v[132:135], v[166:169], v[64:79]
	s_waitcnt lgkmcnt(0)
	v_mfma_f32_32x32x16_bf16 v[80:95], v[144:147], v[174:177], v[80:95]
	v_exp_f32_e32 v144, v120
	v_exp_f32_e32 v145, v121
	v_add_f32_e32 v120, v96, v97
	v_add_f32_e32 v121, v98, v99
	v_exp_f32_e32 v146, v122
	v_add_f32_e32 v120, v120, v121
	v_add_f32_e32 v121, v100, v101
	v_mfma_f32_32x32x16_bf16 v[64:79], v[136:139], v[170:173], v[64:79]
	v_add_f32_e32 v122, v102, v103
	v_exp_f32_e32 v147, v123
	v_add_f32_e32 v121, v121, v122
	v_add_f32_e32 v122, v104, v105
	v_add_f32_e32 v123, v106, v107
	v_add_f32_e32 v122, v122, v123
	v_add_f32_e32 v123, v108, v109
	v_add_f32_e32 v123, v123, v128
	v_add_f32_e32 v128, v112, v113
	v_add_f32_e32 v128, v128, v129
	v_add_f32_e32 v120, v120, v128
	v_add_f32_e32 v128, v116, v117
	v_add_f32_e32 v129, v118, v119
	v_add_f32_e32 v128, v128, v129
	v_add_f32_e32 v121, v121, v128
	v_add_f32_e32 v128, v144, v145
	v_add_f32_e32 v129, v146, v147
	v_mfma_f32_32x32x16_bf16 v[64:79], v[140:143], v[174:177], v[64:79]
	s_movk_i32 s3, 0xffe0
	v_ashrrev_i32_e32 v194, 1, v207
	v_bfi_b32 v194, s3, v194, v207
	v_lshrrev_b32_e32 v195, 1, v207
	v_and_b32_e32 v195, 16, v195
	v_lshl_or_b32 v194, v194, 11, v195
	global_load_dwordx4 v[162:165], v194, s[34:35] offset:128
	global_load_dwordx4 v[166:169], v194, s[34:35] offset:160
	global_load_dwordx4 v[170:173], v194, s[34:35] offset:192
	global_load_dwordx4 v[174:177], v194, s[34:35] offset:224
	v_add_f32_e32 v128, v128, v129
	v_add_f32_e32 v122, v122, v128
	v_add_f32_e32 v128, v124, v125
	v_add_f32_e32 v129, v126, v127
	v_add_f32_e32 v128, v128, v129
	v_add_f32_e32 v123, v123, v128
	v_add_f32_e32 v120, v120, v121
	v_add_f32_e32 v121, v122, v123
	v_add_f32_e32 v128, v120, v121
	v_mov_b32_e32 v129, v128
	v_cvt_pk_bf16_f32 v96, v96, v97
	v_cvt_pk_bf16_f32 v97, v98, v99
	v_cvt_pk_bf16_f32 v98, v100, v101
	v_cvt_pk_bf16_f32 v99, v102, v103
	v_cvt_pk_bf16_f32 v120, v104, v105
	v_cvt_pk_bf16_f32 v121, v106, v107
	v_cvt_pk_bf16_f32 v122, v108, v109
	v_cvt_pk_bf16_f32 v123, v110, v111
	v_cvt_pk_bf16_f32 v104, v112, v113
	v_cvt_pk_bf16_f32 v105, v114, v115
	v_cvt_pk_bf16_f32 v106, v116, v117
	v_cvt_pk_bf16_f32 v107, v118, v119
	v_cvt_pk_bf16_f32 v100, v144, v145
	v_cvt_pk_bf16_f32 v101, v146, v147
	v_cvt_pk_bf16_f32 v102, v124, v125
	v_cvt_pk_bf16_f32 v103, v126, v127
	s_nop 1
	v_permlane32_swap_b32_e32 v128, v129
	v_permlane32_swap_b32_e32 v96, v98
	v_permlane32_swap_b32_e32 v97, v99
	v_permlane32_swap_b32_e32 v120, v122
	v_permlane32_swap_b32_e32 v121, v123
	v_permlane32_swap_b32_e32 v104, v106
	v_permlane32_swap_b32_e32 v105, v107
	v_permlane32_swap_b32_e32 v100, v102
	v_permlane32_swap_b32_e32 v101, v103
	ds_read_b64_tr_b16 v[108:109], v217 offset:0
	ds_read_b64_tr_b16 v[110:111], v217 offset:0x800
	ds_read_b64_tr_b16 v[112:113], v217 offset:0x1000
	ds_read_b64_tr_b16 v[114:115], v217 offset:0x1800
	ds_read_b64_tr_b16 v[116:117], v217 offset:0x2000
	ds_read_b64_tr_b16 v[118:119], v217 offset:0x2800
	ds_read_b64_tr_b16 v[124:125], v217 offset:0x3000
	ds_read_b64_tr_b16 v[126:127], v217 offset:0x3800
	ds_read_b64_tr_b16 v[130:131], v217 offset:0x200
	ds_read_b64_tr_b16 v[132:133], v217 offset:0xa00
	ds_read_b64_tr_b16 v[134:135], v217 offset:0x1200
	ds_read_b64_tr_b16 v[136:137], v217 offset:0x1a00
	ds_read_b64_tr_b16 v[138:139], v217 offset:0x2200
	ds_read_b64_tr_b16 v[140:141], v217 offset:0x2a00
	ds_read_b64_tr_b16 v[142:143], v217 offset:0x3200
	ds_read_b64_tr_b16 v[144:145], v217 offset:0x3a00
	s_waitcnt lgkmcnt(8)
	s_nop 0
	v_mfma_f32_32x32x16_bf16 v[0:15], v[96:99], v[108:111], v[0:15]
	v_max_f32_e32 v108, v81, v81
	v_max_f32_e32 v109, v80, v80
	v_max_f32_e32 v108, v109, v108
	v_max3_f32 v109, v82, v83, v65
	v_max3_f32 v108, v108, v64, v66
	v_max3_f32 v108, v108, v67, v84
	v_max3_f32 v109, v109, v86, v87
	v_mfma_f32_32x32x16_bf16 v[0:15], v[120:123], v[112:115], v[0:15]
	v_max3_f32 v146, v108, v85, v68
	v_max3_f32 v147, v109, v70, v71
	v_mfma_f32_32x32x16_bf16 v[0:15], v[104:107], v[116:119], v[0:15]
	v_mfma_f32_32x32x16_bf16 v[0:15], v[100:103], v[124:127], v[0:15]
	ds_read_b64_tr_b16 v[124:125], v217 offset:0x400
	ds_read_b64_tr_b16 v[126:127], v217 offset:0xc00
	ds_read_b64_tr_b16 v[116:117], v217 offset:0x1400
	ds_read_b64_tr_b16 v[118:119], v217 offset:0x1c00
	ds_read_b64_tr_b16 v[112:113], v217 offset:0x2400
	ds_read_b64_tr_b16 v[114:115], v217 offset:0x2c00
	ds_read_b64_tr_b16 v[108:109], v217 offset:0x3400
	ds_read_b64_tr_b16 v[110:111], v217 offset:0x3c00
	s_waitcnt lgkmcnt(8)
	v_mfma_f32_32x32x16_bf16 v[48:63], v[96:99], v[130:133], v[48:63]
	v_max3_f32 v130, v146, v69, v88
	v_max3_f32 v131, v147, v90, v91
	v_max3_f32 v130, v130, v89, v72
	v_max3_f32 v131, v131, v74, v75
	v_max3_f32 v130, v130, v73, v92
	v_max3_f32 v131, v131, v94, v95
	v_max3_f32 v130, v130, v93, v76
	v_mfma_f32_32x32x16_bf16 v[48:63], v[120:123], v[134:137], v[48:63]
	v_max3_f32 v131, v131, v78, v79
	v_max3_f32 v130, v130, v77, v131
	v_mov_b32_e32 v131, v130
	s_nop 1
	v_permlane32_swap_b32_e32 v130, v131
	v_max_f32_e32 v131, v131, v131
	v_max_f32_e32 v130, v130, v130
	v_mfma_f32_32x32x16_bf16 v[48:63], v[104:107], v[138:141], v[48:63]
	v_max_f32_e32 v131, v130, v131
	v_mfma_f32_32x32x16_bf16 v[48:63], v[100:103], v[142:145], v[48:63]
	s_mov_b32 s2, 0x4138aa3b
	v_cmp_ge_f32_e32 vcc, s2, v131
	s_cmp_lg_u64 vcc, exec
	v_mov_b32_e32 v130, 1.0
	s_cbranch_scc1 .LBB0_868

; #define SBAR() __builtin_amdgcn_sched_barrier(0)
; __device__ __forceinline__ int crow(int r, int hi) { return (r & 3) + 8 * (r >> 2) + 4 * hi; }
; template <int D0> __device__ __forceinline__ void pv_one(f32x16& od, int vb, bf16x8 pa0, bf16x8 pa1, bf16x8 pa2, bf16x8 pa3) {
;     const s16x4 l0 = tr_read<v_rd_off(D0, 0, 0)>(vb), h0 = tr_read<v_rd_off(D0, 0, 1)>(vb), l1 = tr_read<v_rd_off(D0, 1, 0)>(vb), h1 = tr_read<v_rd_off(D0, 1, 1)>(vb);
;     const s16x4 l2 = tr_read<v_rd_off(D0, 2, 0)>(vb), h2 = tr_read<v_rd_off(D0, 2, 1)>(vb), l3 = tr_read<v_rd_off(D0, 3, 0)>(vb), h3 = tr_read<v_rd_off(D0, 3, 1)>(vb);
;     asm volatile("s_waitcnt lgkmcnt(0)" ::: "memory"); SBAR();
;     ...
;     od = __builtin_amdgcn_mfma_f32_32x32x16_bf16(pa0, PK(l0, h0), od, 0, 0, 0);
;     od = __builtin_amdgcn_mfma_f32_32x32x16_bf16(pa1, PK(l1, h1), od, 0, 0, 0);
;     od = __builtin_amdgcn_mfma_f32_32x32x16_bf16(pa2, PK(l2, h2), od, 0, 0, 0);
;     od = __builtin_amdgcn_mfma_f32_32x32x16_bf16(pa3, PK(l3, h3), od, 0, 0, 0);
;     ...
; }
; __device__ __forceinline__ void pv_d0(f32x16* o, int vb, bf16x8 pa0, bf16x8 pa1, bf16x8 pa2, bf16x8 pa3) {
;     pv_one<0>(o[0], vb, pa0, pa1, pa2, pa3); pv_one<1>(o[1], vb, pa0, pa1, pa2, pa3); pv_one<2>(o[2], vb, pa0, pa1, pa2, pa3); pv_one<3>(o[3], vb, pa0, pa1, pa2, pa3);
; __device__ __forceinline__ void diff_pass(const bf16_t* __restrict__ Qb, const bf16_t* __restrict__ Kh, const bf16_t* __restrict__ Vh, int seq, char* lds, f32x16 (&o)[4], const int wave_) {
;     ...
;     FIN(pB0, pB1, alB); SBAR();
;     pv_d0(o, vb0 + s_cur * SHM_V, pa0, pa1, pa2, pa3);
;     if (hi == 0) li_l[r32] = l_reg; asm volatile("s_waitcnt lgkmcnt(0)" ::: "memory");
; #pragma unroll
;     for (int r = 0; r < 16; ++r) { const float rl = __builtin_amdgcn_rcpf(li_l[crow(r, hi)]);
; #pragma unroll
;         for (int d = 0; d < 4; ++d) o[d][r] *= rl; }
.LBB0_843:
	v_exp_f32_e32 v96, v72
	v_exp_f32_e32 v97, v73
	v_add_f32_e32 v72, v80, v81
	v_add_f32_e32 v73, v82, v83
	v_exp_f32_e32 v98, v74
	v_add_f32_e32 v72, v72, v73
	v_add_f32_e32 v73, v84, v85
	v_add_f32_e32 v74, v86, v87
	v_exp_f32_e32 v99, v75
	v_add_f32_e32 v73, v73, v74
	v_add_f32_e32 v74, v88, v89
	v_add_f32_e32 v75, v90, v91
	v_exp_f32_e32 v100, v76
	v_add_f32_e32 v74, v74, v75
	v_add_f32_e32 v75, v92, v93
	v_add_f32_e32 v76, v94, v95
	v_exp_f32_e32 v101, v77
	v_add_f32_e32 v75, v75, v76
	v_add_f32_e32 v76, v64, v65
	v_add_f32_e32 v77, v66, v67
	v_add_f32_e32 v76, v76, v77
	v_exp_f32_e32 v102, v78
	v_exp_f32_e32 v103, v79
	v_add_f32_e32 v72, v72, v76
	v_add_f32_e32 v76, v68, v69
	v_add_f32_e32 v77, v70, v71
	v_add_f32_e32 v76, v76, v77
	v_add_f32_e32 v73, v73, v76
	v_add_f32_e32 v76, v96, v97
	v_add_f32_e32 v77, v98, v99
	v_add_f32_e32 v76, v76, v77
	v_add_f32_e32 v74, v74, v76
	v_add_f32_e32 v76, v100, v101
	v_add_f32_e32 v77, v102, v103
	v_add_f32_e32 v76, v76, v77
	v_add_f32_e32 v75, v75, v76
	v_add_f32_e32 v72, v72, v73
	v_add_f32_e32 v73, v74, v75
	v_add_f32_e32 v72, v72, v73
	v_mov_b32_e32 v73, v72
	s_nop 1
	v_permlane32_swap_b32_e32 v72, v73
	v_cvt_pk_bf16_f32 v74, v80, v81
	v_cvt_pk_bf16_f32 v75, v82, v83
	v_cvt_pk_bf16_f32 v76, v84, v85
	v_cvt_pk_bf16_f32 v77, v86, v87
	v_cvt_pk_bf16_f32 v78, v88, v89
	v_cvt_pk_bf16_f32 v79, v90, v91
	v_cvt_pk_bf16_f32 v80, v92, v93
	v_cvt_pk_bf16_f32 v81, v94, v95
	v_cvt_pk_bf16_f32 v64, v64, v65
	v_cvt_pk_bf16_f32 v65, v66, v67
	v_cvt_pk_bf16_f32 v66, v68, v69
	v_cvt_pk_bf16_f32 v67, v70, v71
	v_cvt_pk_bf16_f32 v68, v96, v97
	v_cvt_pk_bf16_f32 v69, v98, v99
	v_cvt_pk_bf16_f32 v70, v100, v101
	v_cvt_pk_bf16_f32 v71, v102, v103
	s_nop 0
	v_permlane32_swap_b32_e32 v74, v76
	v_permlane32_swap_b32_e32 v75, v77
	v_permlane32_swap_b32_e32 v78, v80
	v_permlane32_swap_b32_e32 v79, v81
	v_permlane32_swap_b32_e32 v64, v66
	v_permlane32_swap_b32_e32 v65, v67
	v_permlane32_swap_b32_e32 v68, v70
	v_permlane32_swap_b32_e32 v69, v71
	s_cmp_lg_u32 0, -1
	s_cselect_b32 s2, 0, 0
	s_addk_i32 s2, 0x4000
	v_add_u32_e32 v98, s2, v216
	ds_read_b64_tr_b16 v[82:83], v98 offset:0
	ds_read_b64_tr_b16 v[84:85], v98 offset:0x800
	ds_read_b64_tr_b16 v[86:87], v98 offset:0x1000
	ds_read_b64_tr_b16 v[88:89], v98 offset:0x1800
	ds_read_b64_tr_b16 v[90:91], v98 offset:0x2000
	ds_read_b64_tr_b16 v[92:93], v98 offset:0x2800
	ds_read_b64_tr_b16 v[94:95], v98 offset:0x3000
	ds_read_b64_tr_b16 v[96:97], v98 offset:0x3800
	s_waitcnt lgkmcnt(0)
	s_nop 0
	v_mfma_f32_32x32x16_bf16 v[0:15], v[74:77], v[82:85], v[0:15]
	ds_read_b64_tr_b16 v[82:83], v98 offset:0x200
	ds_read_b64_tr_b16 v[84:85], v98 offset:0xa00
	v_mfma_f32_32x32x16_bf16 v[0:15], v[78:81], v[86:89], v[0:15]
	ds_read_b64_tr_b16 v[86:87], v98 offset:0x1200
	ds_read_b64_tr_b16 v[88:89], v98 offset:0x1a00
	v_mfma_f32_32x32x16_bf16 v[0:15], v[64:67], v[90:93], v[0:15]
	ds_read_b64_tr_b16 v[90:91], v98 offset:0x2200
	ds_read_b64_tr_b16 v[92:93], v98 offset:0x2a00
	v_mfma_f32_32x32x16_bf16 v[0:15], v[68:71], v[94:97], v[0:15]
	ds_read_b64_tr_b16 v[94:95], v98 offset:0x3200
	ds_read_b64_tr_b16 v[96:97], v98 offset:0x3a00
	s_waitcnt lgkmcnt(0)
	v_mfma_f32_32x32x16_bf16 v[48:63], v[74:77], v[82:85], v[48:63]
	ds_read_b64_tr_b16 v[82:83], v98 offset:0x400
	ds_read_b64_tr_b16 v[84:85], v98 offset:0xc00
	v_mfma_f32_32x32x16_bf16 v[48:63], v[78:81], v[86:89], v[48:63]
	ds_read_b64_tr_b16 v[86:87], v98 offset:0x1400
	ds_read_b64_tr_b16 v[88:89], v98 offset:0x1c00
	v_mfma_f32_32x32x16_bf16 v[48:63], v[64:67], v[90:93], v[48:63]
	ds_read_b64_tr_b16 v[90:91], v98 offset:0x2400
	ds_read_b64_tr_b16 v[92:93], v98 offset:0x2c00
	v_mfma_f32_32x32x16_bf16 v[48:63], v[68:71], v[94:97], v[48:63]
	ds_read_b64_tr_b16 v[94:95], v98 offset:0x3400
	ds_read_b64_tr_b16 v[96:97], v98 offset:0x3c00
	s_waitcnt lgkmcnt(0)
	v_mfma_f32_32x32x16_bf16 v[32:47], v[74:77], v[82:85], v[32:47]
	ds_read_b64_tr_b16 v[82:83], v98 offset:0x600
	ds_read_b64_tr_b16 v[84:85], v98 offset:0xe00
	v_mfma_f32_32x32x16_bf16 v[32:47], v[78:81], v[86:89], v[32:47]
	ds_read_b64_tr_b16 v[86:87], v98 offset:0x1600
	ds_read_b64_tr_b16 v[88:89], v98 offset:0x1e00
	v_mfma_f32_32x32x16_bf16 v[32:47], v[64:67], v[90:93], v[32:47]
	ds_read_b64_tr_b16 v[90:91], v98 offset:0x2600
	ds_read_b64_tr_b16 v[92:93], v98 offset:0x2e00
	v_mfma_f32_32x32x16_bf16 v[32:47], v[68:71], v[94:97], v[32:47]
	ds_read_b64_tr_b16 v[94:95], v98 offset:0x3600
	ds_read_b64_tr_b16 v[96:97], v98 offset:0x3e00
	s_waitcnt lgkmcnt(0)
	v_mfma_f32_32x32x16_bf16 v[16:31], v[74:77], v[82:85], v[16:31]
	v_mfma_f32_32x32x16_bf16 v[16:31], v[78:81], v[86:89], v[16:31]
	v_mfma_f32_32x32x16_bf16 v[16:31], v[64:67], v[90:93], v[16:31]
	v_mfma_f32_32x32x16_bf16 v[16:31], v[68:71], v[94:97], v[16:31]
	s_and_saveexec_b64 s[12:13], s[0:1]
	v_add_f32_e32 v64, v128, v129
	v_fmac_f32_e32 v64, v215, v202
	v_add_f32_e32 v65, v72, v73
	v_fmac_f32_e32 v65, v64, v130
	ds_write_b32 v214, v65
	s_or_b64 exec, exec, s[12:13]
	s_waitcnt lgkmcnt(0)
	v_add_u32_e32 v72, v213, v160
	ds_read_b128 v[64:67], v72
	ds_read_b128 v[68:71], v72 offset:32
	v_ashrrev_i32_e32 v214, 6, v207
	s_add_i32 s0, 0, 0x12800
	v_and_b32_e32 v213, 63, v207
	s_waitcnt lgkmcnt(1)
	v_rcp_f32_e32 v64, v64
	v_rcp_f32_e32 v65, v65
	v_lshl_add_u32 v215, v214, 13, s0
	v_lshl_add_u32 v216, v213, 2, v215
	v_mul_f32_e32 v73, v0, v64
	v_rcp_f32_e32 v0, v66
	v_mul_f32_e32 v48, v48, v64
	v_mul_f32_e32 v32, v32, v64
	v_mul_f32_e32 v16, v16, v64
	v_mul_f32_e32 v64, v1, v65
	v_mul_f32_e32 v49, v49, v65
	v_mul_f32_e32 v33, v33, v65
	v_mul_f32_e32 v17, v17, v65
	v_mul_f32_e32 v65, v2, v0
	v_rcp_f32_e32 v1, v67
	v_mul_f32_e32 v50, v50, v0
	v_mul_f32_e32 v34, v34, v0
	v_mul_f32_e32 v18, v18, v0
	s_waitcnt lgkmcnt(0)
; __device__ __forceinline__ unsigned cvt_pk_bf16(float lo, float hi) { unsigned r; asm volatile("v_cvt_pk_bf16_f32 %0, %1, %2" : "=v"(r) : "v"(lo), "v"(hi)); return r; }
; __device__ __forceinline__ int fresh_lane() { unsigned m = ~0u; asm volatile("" : "+s"(m)); return (int)__builtin_amdgcn_mbcnt_hi(m, __builtin_amdgcn_mbcnt_lo(m, 0u)); }
; __device__ __forceinline__ int v_st(int k, int c) { const int kk = (k & ~0xC) | ((k & 4) << 1) | ((k & 8) >> 1); return ((kk >> 3) * 4 + (c >> 5)) * 512 + ((kk & 7) * 32 + (c & 31)) * 2; }
; __device__ __forceinline__ void diff_pass(const bf16_t* __restrict__ Qb, const bf16_t* __restrict__ Kh, const bf16_t* __restrict__ Vh, int seq, char* lds, f32x16 (&o)[4], const int wave_) {
;     int tid_ = (wave_ << 6) | fresh_lane(); asm volatile("" : "+v"(tid_));
;     const int tid = tid_, wid = tid >> 6, lane = tid & 63, r32 = lane & 31, hi = lane >> 5;
;     char* V_lds = lds; char* K_lds = lds + DA_NBUF * SHM_V;
;     float* ws = (float*)(lds + DA_NBUF * SHM_V + DA_NBUF * SHM_K64) + wid * 64; float* li_l = ws; float* al_l = ws + 32;
;     float m_reg = 0.f, l_reg = 0;
; #pragma unroll
;     for (int d = 0; d < 4; ++d) o[d] = f32x16{};
;     bf16x8 qr[4];
;     const bf16_t* Qw = Qb + (size_t)(wid * 32 + r32) * DM + hi * 8;
; #pragma unroll
;     for (int d0 = 0; d0 < 4; ++d0) qr[d0] = *reinterpret_cast<const bf16x8*>(Qw + d0 * 16);
;     const int sr = tid >> 4, sc = (tid & 15) * 8, vst0 = v_st(sr, sc), vst1 = v_st(32 + sr, sc);
; __device__ __forceinline__ void diff_unit(int b, int h, int qb, const bf16_t* Q, const bf16_t* K, const bf16_t* V, bf16_t* YA, float lam, float omli, const float* subln, char* lds, const int wave_) {
;     ...
;     unsigned* park = (unsigned*)(lds + DA_LDS) + wid * 2048 + lane;
; #pragma unroll
;     for (int d = 0; d < 4; ++d)
; #pragma unroll
;         for (int r = 0; r < 8; ++r) park[(d * 8 + r) * 64] = cvt_pk_bf16(o[d][2 * r], o[d][2 * r + 1]);
	v_rcp_f32_e32 v0, v68
	v_mul_f32_e32 v66, v3, v1
	v_mul_f32_e32 v51, v51, v1
	v_mul_f32_e32 v35, v35, v1
	v_mul_f32_e32 v19, v19, v1
	v_mul_f32_e32 v67, v4, v0
	v_rcp_f32_e32 v1, v69
	v_rcp_f32_e32 v4, v70
	v_rcp_f32_e32 v70, v71
	v_mul_f32_e32 v52, v52, v0
	v_mul_f32_e32 v36, v36, v0
	v_mul_f32_e32 v20, v20, v0
	v_mul_f32_e32 v68, v5, v1
	v_mul_f32_e32 v53, v53, v1
	v_mul_f32_e32 v37, v37, v1
	v_mul_f32_e32 v21, v21, v1
	v_mul_f32_e32 v69, v6, v4
	v_mul_f32_e32 v54, v54, v4
	ds_read_b128 v[0:3], v72 offset:64
	v_mul_f32_e32 v38, v38, v4
	v_mul_f32_e32 v22, v22, v4
	v_mul_f32_e32 v71, v7, v70
	ds_read_b128 v[4:7], v72 offset:96
	s_waitcnt lgkmcnt(1)
	v_rcp_f32_e32 v0, v0
	v_rcp_f32_e32 v1, v1
	v_rcp_f32_e32 v2, v2
	v_rcp_f32_e32 v3, v3
	s_waitcnt lgkmcnt(0)
	v_rcp_f32_e32 v4, v4
	v_rcp_f32_e32 v5, v5
	v_rcp_f32_e32 v6, v6
	v_rcp_f32_e32 v7, v7
	v_mul_f32_e32 v8, v8, v0
	v_mul_f32_e32 v56, v56, v0
	v_mul_f32_e32 v40, v40, v0
	v_mul_f32_e32 v0, v24, v0
	v_mul_f32_e32 v9, v9, v1
	v_mul_f32_e32 v24, v57, v1
	v_mul_f32_e32 v41, v41, v1
	v_mul_f32_e32 v1, v25, v1
	v_mul_f32_e32 v10, v10, v2
	v_mul_f32_e32 v25, v58, v2
	v_mul_f32_e32 v42, v42, v2
	v_mul_f32_e32 v2, v26, v2
	v_mul_f32_e32 v11, v11, v3
	v_mul_f32_e32 v26, v59, v3
	v_mul_f32_e32 v43, v43, v3
	v_mul_f32_e32 v3, v27, v3
	v_mul_f32_e32 v12, v12, v4
	v_mul_f32_e32 v27, v60, v4
	v_mul_f32_e32 v44, v44, v4
	v_mul_f32_e32 v4, v28, v4
	v_mul_f32_e32 v13, v13, v5
	v_mul_f32_e32 v28, v61, v5
	v_mul_f32_e32 v45, v45, v5
	v_mul_f32_e32 v5, v29, v5
	v_mul_f32_e32 v14, v14, v6
	v_mul_f32_e32 v29, v62, v6
	v_mul_f32_e32 v46, v46, v6
	v_mul_f32_e32 v6, v30, v6
	v_mul_f32_e32 v15, v15, v7
	v_mul_f32_e32 v30, v63, v7
	v_mul_f32_e32 v47, v47, v7
	v_mul_f32_e32 v7, v31, v7
	v_cvt_pk_bf16_f32 v31, v73, v64
	ds_write_b32 v216, v31
	v_cvt_pk_bf16_f32 v31, v65, v66
	ds_write_b32 v216, v31 offset:256
	v_cvt_pk_bf16_f32 v31, v67, v68
	ds_write_b32 v216, v31 offset:512
	v_cvt_pk_bf16_f32 v31, v69, v71
	ds_write_b32 v216, v31 offset:768
	v_cvt_pk_bf16_f32 v8, v8, v9
	ds_write_b32 v216, v8 offset:1024
	v_cvt_pk_bf16_f32 v8, v10, v11
	ds_write_b32 v216, v8 offset:1280
	v_cvt_pk_bf16_f32 v8, v12, v13
	ds_write_b32 v216, v8 offset:1536
	v_cvt_pk_bf16_f32 v8, v14, v15
	ds_write_b32 v216, v8 offset:1792
	v_cvt_pk_bf16_f32 v8, v48, v49
	ds_write_b32 v216, v8 offset:2048
	v_cvt_pk_bf16_f32 v8, v50, v51
	ds_write_b32 v216, v8 offset:2304
	v_cvt_pk_bf16_f32 v8, v52, v53
	v_mul_f32_e32 v55, v55, v70
	ds_write_b32 v216, v8 offset:2560
	v_cvt_pk_bf16_f32 v8, v54, v55
	ds_write_b32 v216, v8 offset:2816
	v_cvt_pk_bf16_f32 v8, v56, v24
	ds_write_b32 v216, v8 offset:3072
	v_cvt_pk_bf16_f32 v8, v25, v26
	ds_write_b32 v216, v8 offset:3328
	v_cvt_pk_bf16_f32 v8, v27, v28
	ds_write_b32 v216, v8 offset:3584
	v_cvt_pk_bf16_f32 v8, v29, v30
	ds_write_b32 v216, v8 offset:3840
	v_cvt_pk_bf16_f32 v8, v32, v33
	ds_write_b32 v216, v8 offset:4096
	v_cvt_pk_bf16_f32 v8, v34, v35
	ds_write_b32 v216, v8 offset:4352
	v_cvt_pk_bf16_f32 v8, v36, v37
	v_mul_f32_e32 v39, v39, v70
	ds_write_b32 v216, v8 offset:4608
	v_cvt_pk_bf16_f32 v8, v38, v39
	ds_write_b32 v216, v8 offset:4864
	v_cvt_pk_bf16_f32 v8, v40, v41
	ds_write_b32 v216, v8 offset:5120
	v_cvt_pk_bf16_f32 v8, v42, v43
	ds_write_b32 v216, v8 offset:5376
	v_cvt_pk_bf16_f32 v8, v44, v45
	ds_write_b32 v216, v8 offset:5632
	v_cvt_pk_bf16_f32 v8, v46, v47
	ds_write_b32 v216, v8 offset:5888
	v_cvt_pk_bf16_f32 v8, v16, v17
	ds_write_b32 v216, v8 offset:6144
	v_cvt_pk_bf16_f32 v8, v18, v19
	ds_write_b32 v216, v8 offset:6400
	v_cvt_pk_bf16_f32 v8, v20, v21
	v_mul_f32_e32 v23, v23, v70
	ds_write_b32 v216, v8 offset:6656
	v_cvt_pk_bf16_f32 v8, v22, v23
	ds_write_b32 v216, v8 offset:6912
	v_cvt_pk_bf16_f32 v0, v0, v1
	ds_write_b32 v216, v0 offset:7168
	v_cvt_pk_bf16_f32 v0, v2, v3
	ds_write_b32 v216, v0 offset:7424
	v_cvt_pk_bf16_f32 v0, v4, v5
	ds_write_b32 v216, v0 offset:7680
	v_cvt_pk_bf16_f32 v0, v6, v7
	s_mov_b32 s0, -1
	ds_write_b32 v216, v0 offset:7936
	v_mov_b32_e32 v5, v161
	v_mbcnt_lo_u32_b32 v0, s0, 0
	v_mbcnt_hi_u32_b32 v0, s0, v0
	v_or_b32_e32 v68, s55, v0
	s_movk_i32 s0, 0xffe0
	v_ashrrev_i32_e32 v0, 1, v68
	v_bfi_b32 v0, s0, v0, v68
	v_ashrrev_i32_e32 v1, 31, v0
	v_lshlrev_b64 v[0:1], 11, v[0:1]
	v_lshrrev_b32_e32 v2, 1, v68
	v_ashrrev_i32_e32 v12, 4, v68
	v_lshl_add_u64 v[0:1], s[34:35], 0, v[0:1]
	v_and_b32_e32 v160, 16, v2
	v_lshlrev_b32_e32 v24, 3, v68
	v_ashrrev_i32_e32 v13, 31, v12
	v_lshl_add_u64 v[0:1], v[0:1], 0, v[160:161]
	v_and_b32_e32 v2, 0x78, v24
	v_lshlrev_b64 v[48:49], 11, v[12:13]
	v_lshl_add_u64 v[0:1], s[30:31], 0, v[48:49]
	v_lshlrev_b32_e32 v4, 1, v2
	v_add_u32_e32 v14, 32, v12
	v_ashrrev_i32_e32 v16, 3, v68
	v_lshl_add_u64 v[18:19], v[0:1], 0, v[4:5]
	s_waitcnt lgkmcnt(0)
	s_barrier
; __device__ __forceinline__ int v_st(int k, int c) { const int kk = (k & ~0xC) | ((k & 4) << 1) | ((k & 8) >> 1); return ((kk >> 3) * 4 + (c >> 5)) * 512 + ((kk & 7) * 32 + (c & 31)) * 2; }
; __device__ __forceinline__ int v_rd_base(int lane) { return ((lane & 3) << 3) | (((lane >> 2) & 3) << 6) | (((lane >> 4) & 1) << 5) | (((lane >> 5) & 1) << 8); }
; #define SLOAD(k0) do { vs0 = *reinterpret_cast<const bf16x8*>(&Vh[(size_t)((k0) + sr) * DM + sc]); vs1 = *reinterpret_cast<const bf16x8*>(&Vh[(size_t)((k0) + 32 + sr) * DM + sc]); \
;     ks = *reinterpret_cast<const bf16x8*>(&Kh[(size_t)((k0) + kr) * DM + kc]); } while (0)
; #define SWRITE(s) do { *(bf16x8*)(V_lds + (s) * SHM_V + vst0) = vs0; *(bf16x8*)(V_lds + (s) * SHM_V + vst1) = vs1; *(bf16x8*)(K_lds + (s) * SHM_K64 + kst) = ks; } while (0)
; __device__ __forceinline__ void diff_pass(const bf16_t* __restrict__ Qb, const bf16_t* __restrict__ Kh, const bf16_t* __restrict__ Vh, int seq, char* lds, f32x16 (&o)[4], const int wave_) {
;     ...
;     const int sr = tid >> 4, sc = (tid & 15) * 8, vst0 = v_st(sr, sc), vst1 = v_st(32 + sr, sc);
;     const int kr = tid >> 3, kc = (tid & 7) * 8, kst = kswz<64>(kr, kc * 2);
;     const int vb0 = (int)(uintptr_t)V_lds + v_rd_base(lane);
;     bf16x8 vs0, vs1, ks;
;     ...
;     f32x16 pA0, pA1, pB0, pB1, negm; float alA, alB; bf16x8 pa0, pa1, pa2, pa3; const int NT = seq / 64;
;     int s_prev = 0, s_cur = 0, s_next = 1;
;     __syncthreads();
;     SLOAD(0); SWRITE(0); SLOAD(64); __syncthreads();
;     negm = f32x16{};
;     qkt64c(pA0, pA1, K_lds, qr, negm, r32, hi);
	v_ashrrev_i32_e32 v15, 31, v14
	v_ashrrev_i32_e32 v17, 31, v16
	v_lshlrev_b32_e32 v64, 4, v68
	v_lshlrev_b64 v[6:7], 11, v[14:15]
	v_lshlrev_b64 v[50:51], 11, v[16:17]
	v_lshl_add_u64 v[6:7], s[30:31], 0, v[6:7]
	v_and_b32_e32 v20, 0x70, v64
	v_lshl_add_u64 v[8:9], s[28:29], 0, v[50:51]
	v_mov_b32_e32 v21, v161
	v_lshl_add_u64 v[4:5], v[6:7], 0, v[4:5]
	v_lshl_add_u64 v[22:23], v[8:9], 0, v[20:21]
	v_and_b32_e32 v13, 0xfffff0, v12
	v_lshlrev_b32_e32 v15, 1, v12
	v_and_or_b32 v13, v15, 8, v13
	v_lshrrev_b32_e32 v15, 1, v12
	v_lshrrev_b32_e32 v13, 1, v13
	v_bfe_u32 v17, v24, 5, 2
	v_and_b32_e32 v12, 3, v12
	v_or_b32_e32 v13, v13, v17
	v_and_or_b32 v12, v15, 4, v12
	v_lshlrev_b32_e32 v13, 9, v13
	v_lshlrev_b32_e32 v12, 6, v12
	v_and_b32_e32 v15, 48, v64
	v_or3_b32 v222, v13, v12, v15
	v_and_b32_e32 v13, 0xfffff0, v14
	v_lshlrev_b32_e32 v14, 1, v14
	v_and_or_b32 v13, v14, 8, v13
	v_lshrrev_b32_e32 v13, 1, v13
	v_or_b32_e32 v13, v13, v17
	v_add_u32_e32 v70, 0, v222
	s_mov_b32 s0, 0x20000
	v_lshlrev_b32_e32 v13, 9, v13
	v_or3_b32 v223, v13, v12, v15
	v_lshlrev_b32_e32 v12, 7, v16
	v_and_b32_e32 v13, 0x70, v68
	s_mov_b32 s1, 0x30000
	v_bitop3_b32 v224, v20, v12, v13 bitop3:0xde
	v_add_u32_e32 v71, 0, v223
	v_add_u32_e32 v225, 0, v224
	v_and_b32_e32 v69, 31, v68
	v_lshlrev_b32_e32 v12, 7, v69
	v_and_b32_e32 v13, 0x70, v24
	v_bitop3_b32 v227, v160, v12, v13 bitop3:0xde
	v_add_u32_e32 v226, 0, v227
	v_and_b32_e32 v72, 63, v68
	s_mov_b32 s12, 0
	s_mov_b32 s13, s12
	s_mov_b32 s14, s12
	s_mov_b32 s15, s12
	s_mov_b32 s16, s12
	s_mov_b32 s17, s12
	s_mov_b32 s18, s12
	s_mov_b32 s19, s12
	s_mov_b32 s20, s12
	s_mov_b32 s21, s12
	s_mov_b32 s22, s12
	s_mov_b32 s23, s12
	s_mov_b32 s24, s12
	s_mov_b32 s25, s12
	s_mov_b32 s26, s12
	s_mov_b32 s27, s12
	s_cmp_lg_u32 0, -1
	s_mov_b32 s29, 2
	s_mov_b32 s28, -1
	s_mov_b32 s30, 1
	v_mov_b32_e32 v234, 1.0
	v_mov_b32_e32 v219, 0
	s_waitcnt vmcnt(0)
	ds_write_b128 v70, v[178:181]
	v_add_co_u32_e32 v0, vcc, s0, v18
	s_nop 1
	v_addc_co_u32_e32 v1, vcc, 0, v19, vcc
	global_load_dwordx4 v[52:55], v[0:1], off
	v_add_co_u32_e32 v0, vcc, s1, v18
	s_waitcnt vmcnt(2)
	ds_write_b128 v71, v[182:185]
	v_addc_co_u32_e32 v1, vcc, 0, v19, vcc
	s_waitcnt vmcnt(1)
	ds_write_b128 v225, v[186:189] offset:49152
	v_add_co_u32_e32 v2, vcc, s0, v22
	v_and_b32_e32 v8, 0x3fffffc0, v68
	s_nop 0
	v_addc_co_u32_e32 v3, vcc, 0, v23, vcc
	global_load_dwordx4 v[56:59], v[0:1], off
	global_load_dwordx4 v[60:63], v[2:3], off offset:128
	s_waitcnt lgkmcnt(0)
	s_barrier
	ds_read_b128 v[0:3], v226 offset:49152
	ds_read_b128 v[4:7], v226 offset:53248
	s_waitcnt lgkmcnt(1)
	v_mfma_f32_32x32x16_bf16 v[32:47], v[0:3], v[162:165], 0
	v_or_b32_e32 v0, 32, v160
	v_bitop3_b32 v231, v0, v12, v13 bitop3:0xde
	v_add_u32_e32 v228, 0, v231
	v_lshl_add_u32 v217, v8, 2, s39
	s_cselect_b32 s0, 0, 0
	v_lshl_add_u32 v218, v69, 2, v217
	s_waitcnt lgkmcnt(0)
	v_mfma_f32_32x32x16_bf16 v[16:31], v[4:7], v[162:165], 0
	ds_read_b128 v[0:3], v228 offset:49152
	ds_read_b128 v[4:7], v228 offset:53248
	s_waitcnt lgkmcnt(1)
	v_mfma_f32_32x32x16_bf16 v[32:47], v[0:3], v[166:169], v[32:47]
	v_or_b32_e32 v0, 64, v160
	v_bitop3_b32 v232, v0, v12, v13 bitop3:0xde
	v_add_u32_e32 v229, 0, v232
	ds_read_b128 v[0:3], v229 offset:53248
	ds_read_b128 v[8:11], v229 offset:49152
	s_waitcnt lgkmcnt(2)
	v_mfma_f32_32x32x16_bf16 v[16:31], v[4:7], v[166:169], v[16:31]
	v_lshlrev_b32_e32 v4, 3, v72
	v_and_b32_e32 v5, 0xc0, v64
	v_lshlrev_b32_e32 v6, 1, v68
	v_and_or_b32 v5, v4, 24, v5
	v_and_b32_e32 v6, 32, v6
	v_and_b32_e32 v4, 0x100, v4
	v_or3_b32 v220, v5, v6, v4
	s_waitcnt lgkmcnt(0)
	v_mfma_f32_32x32x16_bf16 v[32:47], v[8:11], v[170:173], v[32:47]
	v_or_b32_e32 v4, 0x60, v160
	v_bitop3_b32 v233, v4, v12, v13 bitop3:0xde
	v_add_u32_e32 v230, 0, v233
	ds_read_b128 v[64:67], v230 offset:53248
	ds_read_b128 v[4:7], v230 offset:49152
	s_waitcnt vmcnt(2)
	ds_write_b128 v70, v[52:55] offset:16384
	s_waitcnt vmcnt(1)
	ds_write_b128 v71, v[56:59] offset:16384
	s_waitcnt vmcnt(0)
	ds_write_b128 v225, v[60:63] offset:57344
	v_mfma_f32_32x32x16_bf16 v[16:31], v[0:3], v[170:173], v[16:31]
	v_add_u32_e32 v221, s0, v220
	v_cmp_gt_u32_e64 s[0:1], 32, v72
	s_waitcnt lgkmcnt(0)
	s_barrier
; #define MX3(a, b, c) __builtin_fmaxf(__builtin_fmaxf((a), (b)), (c))
; #define EX2(x) x = __builtin_amdgcn_exp2f(x)
; #define MX3(a, b, c) __builtin_fmaxf(__builtin_fmaxf((a), (b)), (c))
; __device__ __forceinline__ void qkt64c(f32x16& p0, f32x16& p1, const char* Ks, const bf16x8* qr, const f32x16& cinit, int r32, int hi) {
; #pragma unroll
;     for (int d0 = 0; d0 < 4; ++d0) { const int cb = (d0 * 16 + hi * 8) * 2;
;         const bf16x8 b0 = *reinterpret_cast<const bf16x8*>(Ks + kswz<64>(r32, cb));
;         const bf16x8 b1 = *reinterpret_cast<const bf16x8*>(Ks + kswz<64>(32 + r32, cb));
;         if (d0 == 0) { p0 = __builtin_amdgcn_mfma_f32_32x32x16_bf16(b0, qr[0], cinit, 0, 0, 0); p1 = __builtin_amdgcn_mfma_f32_32x32x16_bf16(b1, qr[0], cinit, 0, 0, 0); }
;         else { p0 = __builtin_amdgcn_mfma_f32_32x32x16_bf16(b0, qr[d0], p0, 0, 0, 0); p1 = __builtin_amdgcn_mfma_f32_32x32x16_bf16(b1, qr[d0], p1, 0, 0, 0); } }
; }
; __device__ __forceinline__ float rowmax32(const f32x16& p0, const f32x16& p1) {
;     ...
;     float a = MX3(p0[0], p0[1], p1[0]), b = MX3(p0[2], p0[3], p1[1]); a = MX3(a, p1[2], p1[3]);
; #pragma unroll
;     for (int r = 4; r < 16; r += 4) { a = MX3(a, p0[r], p0[r + 1]); b = MX3(b, p0[r + 2], p0[r + 3]); a = MX3(a, p1[r], p1[r + 1]); b = MX3(b, p1[r + 2], p1[r + 3]); }
;     ...
;     float m = __builtin_fmaxf(a, b);
;     auto rr = __builtin_amdgcn_permlane32_swap(__float_as_uint(m), __float_as_uint(m), false, false);
;     return __builtin_fmaxf(__uint_as_float(rr[0]), __uint_as_float(rr[1]));
; }
; __device__ __forceinline__ void diff_pass(const bf16_t* __restrict__ Qb, const bf16_t* __restrict__ Kh, const bf16_t* __restrict__ Vh, int seq, char* lds, f32x16 (&o)[4], const int wave_) {
;     ...
;     negm = f32x16{};
;     qkt64c(pA0, pA1, K_lds, qr, negm, r32, hi);
;     { const float pm = rowmax32(pA0, pA1); m_reg = pm; alA = 1.f;
; #pragma unroll
;       for (int r = 0; r < 16; ++r) { pA0[r] -= pm; pA1[r] -= pm; negm[r] = -pm; }
; #pragma unroll
;       for (int r = 0; r < 16; ++r) EX2(pA0[r]);
; #pragma unroll
;       for (int r = 0; r < 8; ++r) EX2(pA1[r]); }
	v_mfma_f32_32x32x16_bf16 v[32:47], v[4:7], v[174:177], v[32:47]
	v_mov_b64_e32 v[0:1], s[12:13]
	v_mov_b64_e32 v[14:15], s[26:27]
	v_mov_b64_e32 v[2:3], s[14:15]
	v_mov_b64_e32 v[4:5], s[16:17]
	v_mov_b64_e32 v[6:7], s[18:19]
	v_mov_b64_e32 v[8:9], s[20:21]
	v_mov_b64_e32 v[10:11], s[22:23]
	v_mfma_f32_32x32x16_bf16 v[16:31], v[64:67], v[174:177], v[16:31]
	s_nop 3
	v_max_f32_e32 v64, v33, v33
	v_max_f32_e32 v65, v32, v32
	v_max_f32_e32 v64, v65, v64
	v_mov_b64_e32 v[12:13], s[24:25]
	s_nop 3
	v_max3_f32 v65, v34, v35, v17
	v_max3_f32 v64, v64, v16, v18
	v_max3_f32 v64, v64, v19, v36
	v_max3_f32 v65, v65, v38, v39
	v_max3_f32 v64, v64, v37, v20
	v_max3_f32 v65, v65, v22, v23
	v_max3_f32 v64, v64, v21, v40
	v_max3_f32 v65, v65, v42, v43
	v_max3_f32 v64, v64, v41, v24
	v_max3_f32 v65, v65, v26, v27
	v_max3_f32 v64, v64, v25, v44
	v_max3_f32 v65, v65, v46, v47
	v_max3_f32 v64, v64, v45, v28
	v_max3_f32 v65, v65, v30, v31
	v_max3_f32 v64, v64, v29, v65
	v_mov_b32_e32 v65, v64
	s_nop 1
	v_permlane32_swap_b32_e32 v64, v65
	v_max_f32_e32 v65, v65, v65
	v_max_f32_e32 v64, v64, v64
	v_max_f32_e32 v196, v64, v65
	v_sub_f32_e32 v18, v18, v196
	v_sub_f32_e32 v16, v16, v196
	v_sub_f32_e32 v17, v17, v196
	v_sub_f32_e32 v19, v19, v196
	v_exp_f32_e32 v114, v18
	v_and_b32_e32 v18, 7, v68
	v_exp_f32_e32 v112, v16
	v_exp_f32_e32 v113, v17
	v_exp_f32_e32 v115, v19
	v_lshl_add_u64 v[16:17], s[10:11], 0, v[50:51]
	v_lshlrev_b32_e32 v18, 4, v18
	v_mov_b32_e32 v19, v161
	v_sub_f32_e32 v32, v32, v196
	v_sub_f32_e32 v33, v33, v196
	v_sub_f32_e32 v34, v34, v196
	v_sub_f32_e32 v35, v35, v196
	v_sub_f32_e32 v36, v36, v196
	v_sub_f32_e32 v20, v20, v196
	v_sub_f32_e32 v37, v37, v196
	v_sub_f32_e32 v21, v21, v196
	v_sub_f32_e32 v38, v38, v196
	v_sub_f32_e32 v22, v22, v196
	v_sub_f32_e32 v39, v39, v196
	v_sub_f32_e32 v23, v23, v196
	v_sub_f32_e32 v40, v40, v196
	v_sub_f32_e32 v41, v41, v196
	v_pk_add_f32 v[120:121], v[24:25], v[196:197] op_sel_hi:[1,0] neg_lo:[0,1] neg_hi:[0,1]
	v_sub_f32_e32 v24, v42, v196
	v_sub_f32_e32 v25, v43, v196
	v_pk_add_f32 v[122:123], v[26:27], v[196:197] op_sel_hi:[1,0] neg_lo:[0,1] neg_hi:[0,1]
	v_sub_f32_e32 v26, v44, v196
	v_sub_f32_e32 v27, v45, v196
	v_pk_add_f32 v[124:125], v[28:29], v[196:197] op_sel_hi:[1,0] neg_lo:[0,1] neg_hi:[0,1]
	v_sub_f32_e32 v28, v46, v196
	v_sub_f32_e32 v29, v47, v196
	v_lshl_add_u64 v[16:17], v[16:17], 0, v[18:19]
	v_and_b32_e32 v18, 15, v68
	v_exp_f32_e32 v96, v32
	v_exp_f32_e32 v97, v33
	v_exp_f32_e32 v98, v34
	v_exp_f32_e32 v99, v35
	v_exp_f32_e32 v100, v36
	v_exp_f32_e32 v101, v37
	v_exp_f32_e32 v102, v38
	v_exp_f32_e32 v103, v39
	v_exp_f32_e32 v104, v40
	v_exp_f32_e32 v105, v41
	v_exp_f32_e32 v106, v24
	v_exp_f32_e32 v107, v25
	v_exp_f32_e32 v108, v26
	v_exp_f32_e32 v109, v27
	v_exp_f32_e32 v110, v28
	v_exp_f32_e32 v111, v29
	v_exp_f32_e32 v116, v20
	v_exp_f32_e32 v117, v21
	v_exp_f32_e32 v118, v22
	v_exp_f32_e32 v119, v23
	v_lshl_add_u64 v[198:199], s[52:53], 0, v[16:17]
	v_lshl_add_u64 v[16:17], s[10:11], 0, v[48:49]
	v_lshlrev_b32_e32 v18, 4, v18
	v_lshl_add_u64 v[16:17], v[16:17], 0, v[18:19]
	v_xor_b32_e32 v80, 0x80000000, v196
	v_pk_add_f32 v[126:127], v[30:31], v[196:197] op_sel_hi:[1,0] neg_lo:[0,1] neg_hi:[0,1]
	v_lshl_add_u64 v[200:201], s[52:53], 0, v[16:17]
	v_mov_b64_e32 v[62:63], v[14:15]
	v_mov_b64_e32 v[46:47], v[14:15]
	v_mov_b64_e32 v[30:31], v[14:15]
	v_mov_b64_e32 v[60:61], v[12:13]
	v_mov_b64_e32 v[58:59], v[10:11]
	v_mov_b64_e32 v[56:57], v[8:9]
	v_mov_b64_e32 v[54:55], v[6:7]
	v_mov_b64_e32 v[52:53], v[4:5]
	v_mov_b64_e32 v[50:51], v[2:3]
	v_mov_b64_e32 v[48:49], v[0:1]
	v_mov_b64_e32 v[44:45], v[12:13]
	v_mov_b64_e32 v[42:43], v[10:11]
	v_mov_b64_e32 v[40:41], v[8:9]
	v_mov_b64_e32 v[38:39], v[6:7]
	v_mov_b64_e32 v[36:37], v[4:5]
	v_mov_b64_e32 v[34:35], v[2:3]
	v_mov_b64_e32 v[32:33], v[0:1]
	v_mov_b64_e32 v[28:29], v[12:13]
	v_mov_b64_e32 v[26:27], v[10:11]
	v_mov_b64_e32 v[24:25], v[8:9]
	v_mov_b64_e32 v[22:23], v[6:7]
	v_mov_b64_e32 v[20:21], v[4:5]
	v_mov_b64_e32 v[18:19], v[2:3]
	v_mov_b64_e32 v[16:17], v[0:1]
	v_mov_b32_e32 v81, v80
	v_mov_b32_e32 v82, v80
	v_mov_b32_e32 v83, v80
	v_mov_b32_e32 v84, v80
	v_mov_b32_e32 v85, v80
	v_mov_b32_e32 v86, v80
	v_mov_b32_e32 v87, v80
	v_mov_b32_e32 v88, v80
	v_mov_b32_e32 v89, v80
	v_mov_b32_e32 v90, v80
	v_mov_b32_e32 v91, v80
	v_mov_b32_e32 v92, v80
	v_mov_b32_e32 v93, v80
	v_mov_b32_e32 v94, v80
	v_mov_b32_e32 v95, v80
